# sc1 write-through on P1/P4 GEMM epilogue dwordx4 stores
# baseline (speedup 1.0000x reference)
.LBB0_166:
	v_lshl_add_u32 v177, s40, 8, v1
	v_lshl_or_b32 v122, s38, 8, v175
	v_mov_b64_e32 v[124:125], s[8:9]
	v_ashrrev_i32_e32 v123, 31, v122
	v_mad_i64_i32 v[124:125], s[38:39], v177, s69, v[124:125]
	v_lshl_add_u64 v[124:125], v[122:123], 1, v[124:125]
	v_cvt_pk_bf16_f32 v126, v154, v155
	v_cvt_pk_bf16_f32 v127, v150, v151
	v_cvt_pk_bf16_f32 v128, v156, v157
	v_cvt_pk_bf16_f32 v129, v152, v153
	s_cmp_gt_i32 s29, 1
	s_mov_b64 s[38:39], -1
	global_store_dwordx4 v[124:125], v[126:129], off sc1
	s_cbranch_scc0 .LBB0_168
	s_nop 0
	v_mul_f32_e32 v126, 0xbfb8aa3b, v118
	v_exp_f32_e32 v126, v126
	v_mul_f32_e32 v127, 0xbfb8aa3b, v114
	v_mul_f32_e32 v128, 0xbfb8aa3b, v119
	v_exp_f32_e32 v127, v127
	v_exp_f32_e32 v129, v128
	v_add_f32_e32 v126, 1.0, v126
	v_rcp_f32_e32 v128, v126
	v_add_f32_e32 v126, 1.0, v127
	v_rcp_f32_e32 v152, v126
	v_add_f32_e32 v126, 1.0, v129
	v_rcp_f32_e32 v129, v126
	v_mul_f32_e32 v126, 0xbfb8aa3b, v115
	v_mul_f32_e32 v127, 0xbfb8aa3b, v120
	v_mul_f32_e32 v150, 0xbfb8aa3b, v116
	v_exp_f32_e32 v126, v126
	v_exp_f32_e32 v127, v127
	v_exp_f32_e32 v150, v150
	v_mul_f32_e32 v153, 0xbfb8aa3b, v117
	v_add_f32_e32 v151, 1.0, v126
	v_add_f32_e32 v126, 1.0, v127
	v_add_f32_e32 v127, 1.0, v150
	v_mul_f32_e32 v150, 0xbfb8aa3b, v121
	v_exp_f32_e32 v150, v150
	v_exp_f32_e32 v153, v153
	v_rcp_f32_e32 v154, v127
	v_rcp_f32_e32 v126, v126
	v_add_f32_e32 v127, 1.0, v150
	v_add_f32_e32 v150, 1.0, v153
	v_rcp_f32_e32 v127, v127
	v_rcp_f32_e32 v155, v150
	v_rcp_f32_e32 v153, v151
	v_pk_mul_f32 v[150:151], v[118:119], v[128:129]
	v_pk_mul_f32 v[126:127], v[120:121], v[126:127]
	v_pk_mul_f32 v[128:129], v[116:117], v[154:155]
	v_pk_mul_f32 v[152:153], v[114:115], v[152:153]
	s_mov_b64 s[38:39], 0

.LBB0_172:
	v_cvt_pk_bf16_f32 v114, v150, v151
	v_cvt_pk_bf16_f32 v115, v126, v127
	v_cvt_pk_bf16_f32 v116, v152, v153
	v_cvt_pk_bf16_f32 v117, v128, v129
	s_cmp_gt_i32 s29, 1
	s_mov_b64 s[38:39], -1
	global_store_dwordx4 v[124:125], v[114:117], off offset:256 sc1
	s_cbranch_scc0 .LBB0_174
	s_nop 0
	v_mul_f32_e32 v114, 0xbfb8aa3b, v110
	v_exp_f32_e32 v114, v114
	v_mul_f32_e32 v115, 0xbfb8aa3b, v106
	v_mul_f32_e32 v116, 0xbfb8aa3b, v111
	v_exp_f32_e32 v115, v115
	v_exp_f32_e32 v117, v116
	v_add_f32_e32 v114, 1.0, v114
	v_rcp_f32_e32 v116, v114
	v_add_f32_e32 v114, 1.0, v115
	v_rcp_f32_e32 v120, v114
	v_add_f32_e32 v114, 1.0, v117
	v_rcp_f32_e32 v117, v114
	v_mul_f32_e32 v114, 0xbfb8aa3b, v107
	v_mul_f32_e32 v115, 0xbfb8aa3b, v112
	v_mul_f32_e32 v118, 0xbfb8aa3b, v108
	v_exp_f32_e32 v114, v114
	v_exp_f32_e32 v115, v115
	v_exp_f32_e32 v118, v118
	v_mul_f32_e32 v121, 0xbfb8aa3b, v109
	v_add_f32_e32 v119, 1.0, v114
	v_add_f32_e32 v114, 1.0, v115
	v_add_f32_e32 v115, 1.0, v118
	v_mul_f32_e32 v118, 0xbfb8aa3b, v113
	v_exp_f32_e32 v118, v118
	v_exp_f32_e32 v121, v121
	v_rcp_f32_e32 v124, v115
	v_rcp_f32_e32 v114, v114
	v_add_f32_e32 v115, 1.0, v118
	v_add_f32_e32 v118, 1.0, v121
	v_rcp_f32_e32 v115, v115
	v_rcp_f32_e32 v125, v118
	v_rcp_f32_e32 v121, v119
	v_pk_mul_f32 v[118:119], v[110:111], v[116:117]
	v_pk_mul_f32 v[114:115], v[112:113], v[114:115]
	v_pk_mul_f32 v[116:117], v[108:109], v[124:125]
	v_pk_mul_f32 v[120:121], v[106:107], v[120:121]
	s_mov_b64 s[38:39], 0

.LBB0_178:
	v_or_b32_e32 v108, 16, v177
	v_mov_b64_e32 v[106:107], s[8:9]
	v_mad_i64_i32 v[106:107], s[38:39], v108, s69, v[106:107]
	v_lshl_add_u64 v[106:107], v[122:123], 1, v[106:107]
	v_cvt_pk_bf16_f32 v108, v118, v119
	v_cvt_pk_bf16_f32 v109, v114, v115
	v_cvt_pk_bf16_f32 v110, v120, v121
	v_cvt_pk_bf16_f32 v111, v116, v117
	s_cmp_gt_i32 s29, 1
	s_mov_b64 s[38:39], -1
	global_store_dwordx4 v[106:107], v[108:111], off sc1
	s_cbranch_scc0 .LBB0_180
	s_nop 0
	v_mul_f32_e32 v108, 0xbfb8aa3b, v102
	v_exp_f32_e32 v108, v108
	v_mul_f32_e32 v109, 0xbfb8aa3b, v98
	v_mul_f32_e32 v110, 0xbfb8aa3b, v103
	v_exp_f32_e32 v109, v109
	v_exp_f32_e32 v111, v110
	v_add_f32_e32 v108, 1.0, v108
	v_rcp_f32_e32 v110, v108
	v_add_f32_e32 v108, 1.0, v109
	v_rcp_f32_e32 v114, v108
	v_add_f32_e32 v108, 1.0, v111
	v_rcp_f32_e32 v111, v108
	v_mul_f32_e32 v108, 0xbfb8aa3b, v99
	v_mul_f32_e32 v109, 0xbfb8aa3b, v104
	v_mul_f32_e32 v112, 0xbfb8aa3b, v100
	v_exp_f32_e32 v108, v108
	v_exp_f32_e32 v109, v109
	v_exp_f32_e32 v112, v112
	v_mul_f32_e32 v115, 0xbfb8aa3b, v101
	v_add_f32_e32 v113, 1.0, v108
	v_add_f32_e32 v108, 1.0, v109
	v_add_f32_e32 v109, 1.0, v112
	v_mul_f32_e32 v112, 0xbfb8aa3b, v105
	v_exp_f32_e32 v112, v112
	v_exp_f32_e32 v115, v115
	v_rcp_f32_e32 v116, v109
	v_rcp_f32_e32 v108, v108
	v_add_f32_e32 v109, 1.0, v112
	v_add_f32_e32 v112, 1.0, v115
	v_rcp_f32_e32 v109, v109
	v_rcp_f32_e32 v117, v112
	v_rcp_f32_e32 v115, v113
	v_pk_mul_f32 v[112:113], v[102:103], v[110:111]
	v_pk_mul_f32 v[108:109], v[104:105], v[108:109]
	v_pk_mul_f32 v[110:111], v[100:101], v[116:117]
	v_pk_mul_f32 v[114:115], v[98:99], v[114:115]
	s_mov_b64 s[38:39], 0

.LBB0_184:
	v_cvt_pk_bf16_f32 v98, v112, v113
	v_cvt_pk_bf16_f32 v99, v108, v109
	v_cvt_pk_bf16_f32 v100, v114, v115
	v_cvt_pk_bf16_f32 v101, v110, v111
	s_cmp_gt_i32 s29, 1
	s_mov_b64 s[38:39], -1
	global_store_dwordx4 v[106:107], v[98:101], off offset:256 sc1
	s_cbranch_scc0 .LBB0_186
	s_nop 0
	v_mul_f32_e32 v98, 0xbfb8aa3b, v94
	v_exp_f32_e32 v98, v98
	v_mul_f32_e32 v99, 0xbfb8aa3b, v90
	v_mul_f32_e32 v100, 0xbfb8aa3b, v95
	v_exp_f32_e32 v99, v99
	v_exp_f32_e32 v101, v100
	v_add_f32_e32 v98, 1.0, v98
	v_rcp_f32_e32 v100, v98
	v_add_f32_e32 v98, 1.0, v99
	v_rcp_f32_e32 v104, v98
	v_add_f32_e32 v98, 1.0, v101
	v_rcp_f32_e32 v101, v98
	v_mul_f32_e32 v98, 0xbfb8aa3b, v91
	v_mul_f32_e32 v99, 0xbfb8aa3b, v96
	v_mul_f32_e32 v102, 0xbfb8aa3b, v92
	v_exp_f32_e32 v98, v98
	v_exp_f32_e32 v99, v99
	v_exp_f32_e32 v102, v102
	v_mul_f32_e32 v105, 0xbfb8aa3b, v93
	v_add_f32_e32 v103, 1.0, v98
	v_add_f32_e32 v98, 1.0, v99
	v_add_f32_e32 v99, 1.0, v102
	v_mul_f32_e32 v102, 0xbfb8aa3b, v97
	v_exp_f32_e32 v102, v102
	v_exp_f32_e32 v105, v105
	v_rcp_f32_e32 v106, v99
	v_rcp_f32_e32 v98, v98
	v_add_f32_e32 v99, 1.0, v102
	v_add_f32_e32 v102, 1.0, v105
	v_rcp_f32_e32 v99, v99
	v_rcp_f32_e32 v107, v102
	v_rcp_f32_e32 v105, v103
	v_pk_mul_f32 v[102:103], v[94:95], v[100:101]
	v_pk_mul_f32 v[98:99], v[96:97], v[98:99]
	v_pk_mul_f32 v[100:101], v[92:93], v[106:107]
	v_pk_mul_f32 v[104:105], v[90:91], v[104:105]
	s_mov_b64 s[38:39], 0

.LBB0_190:
	v_or_b32_e32 v92, 32, v177
	v_mov_b64_e32 v[90:91], s[8:9]
	v_mad_i64_i32 v[90:91], s[38:39], v92, s69, v[90:91]
	v_lshl_add_u64 v[90:91], v[122:123], 1, v[90:91]
	v_cvt_pk_bf16_f32 v92, v102, v103
	v_cvt_pk_bf16_f32 v93, v98, v99
	v_cvt_pk_bf16_f32 v94, v104, v105
	v_cvt_pk_bf16_f32 v95, v100, v101
	s_cmp_gt_i32 s29, 1
	s_mov_b64 s[38:39], -1
	global_store_dwordx4 v[90:91], v[92:95], off sc1
	s_cbranch_scc0 .LBB0_192
	s_nop 0
	v_mul_f32_e32 v92, 0xbfb8aa3b, v86
	v_exp_f32_e32 v92, v92
	v_mul_f32_e32 v93, 0xbfb8aa3b, v82
	v_mul_f32_e32 v94, 0xbfb8aa3b, v87
	v_exp_f32_e32 v93, v93
	v_exp_f32_e32 v95, v94
	v_add_f32_e32 v92, 1.0, v92
	v_rcp_f32_e32 v94, v92
	v_add_f32_e32 v92, 1.0, v93
	v_rcp_f32_e32 v98, v92
	v_add_f32_e32 v92, 1.0, v95
	v_rcp_f32_e32 v95, v92
	v_mul_f32_e32 v92, 0xbfb8aa3b, v83
	v_mul_f32_e32 v93, 0xbfb8aa3b, v88
	v_mul_f32_e32 v96, 0xbfb8aa3b, v84
	v_exp_f32_e32 v92, v92
	v_exp_f32_e32 v93, v93
	v_exp_f32_e32 v96, v96
	v_mul_f32_e32 v99, 0xbfb8aa3b, v85
	v_add_f32_e32 v97, 1.0, v92
	v_add_f32_e32 v92, 1.0, v93
	v_add_f32_e32 v93, 1.0, v96
	v_mul_f32_e32 v96, 0xbfb8aa3b, v89
	v_exp_f32_e32 v96, v96
	v_exp_f32_e32 v99, v99
	v_rcp_f32_e32 v100, v93
	v_rcp_f32_e32 v92, v92
	v_add_f32_e32 v93, 1.0, v96
	v_add_f32_e32 v96, 1.0, v99
	v_rcp_f32_e32 v93, v93
	v_rcp_f32_e32 v101, v96
	v_rcp_f32_e32 v99, v97
	v_pk_mul_f32 v[96:97], v[86:87], v[94:95]
	v_pk_mul_f32 v[92:93], v[88:89], v[92:93]
	v_pk_mul_f32 v[94:95], v[84:85], v[100:101]
	v_pk_mul_f32 v[98:99], v[82:83], v[98:99]
	s_mov_b64 s[38:39], 0

.LBB0_196:
	v_cvt_pk_bf16_f32 v82, v96, v97
	v_cvt_pk_bf16_f32 v83, v92, v93
	v_cvt_pk_bf16_f32 v84, v98, v99
	v_cvt_pk_bf16_f32 v85, v94, v95
	s_cmp_gt_i32 s29, 1
	s_mov_b64 s[38:39], -1
	global_store_dwordx4 v[90:91], v[82:85], off offset:256 sc1
	s_cbranch_scc0 .LBB0_198
	s_nop 0
	v_mul_f32_e32 v82, 0xbfb8aa3b, v78
	v_exp_f32_e32 v82, v82
	v_mul_f32_e32 v83, 0xbfb8aa3b, v74
	v_mul_f32_e32 v84, 0xbfb8aa3b, v79
	v_exp_f32_e32 v83, v83
	v_exp_f32_e32 v85, v84
	v_add_f32_e32 v82, 1.0, v82
	v_rcp_f32_e32 v84, v82
	v_add_f32_e32 v82, 1.0, v83
	v_rcp_f32_e32 v88, v82
	v_add_f32_e32 v82, 1.0, v85
	v_rcp_f32_e32 v85, v82
	v_mul_f32_e32 v82, 0xbfb8aa3b, v75
	v_mul_f32_e32 v83, 0xbfb8aa3b, v80
	v_mul_f32_e32 v86, 0xbfb8aa3b, v76
	v_exp_f32_e32 v82, v82
	v_exp_f32_e32 v83, v83
	v_exp_f32_e32 v86, v86
	v_mul_f32_e32 v89, 0xbfb8aa3b, v77
	v_add_f32_e32 v87, 1.0, v82
	v_add_f32_e32 v82, 1.0, v83
	v_add_f32_e32 v83, 1.0, v86
	v_mul_f32_e32 v86, 0xbfb8aa3b, v81
	v_exp_f32_e32 v86, v86
	v_exp_f32_e32 v89, v89
	v_rcp_f32_e32 v90, v83
	v_rcp_f32_e32 v82, v82
	v_add_f32_e32 v83, 1.0, v86
	v_add_f32_e32 v86, 1.0, v89
	v_rcp_f32_e32 v83, v83
	v_rcp_f32_e32 v91, v86
	v_rcp_f32_e32 v89, v87
	v_pk_mul_f32 v[86:87], v[78:79], v[84:85]
	v_pk_mul_f32 v[82:83], v[80:81], v[82:83]
	v_pk_mul_f32 v[84:85], v[76:77], v[90:91]
	v_pk_mul_f32 v[88:89], v[74:75], v[88:89]
	s_mov_b64 s[38:39], 0

.LBB0_202:
	v_or_b32_e32 v76, 48, v177
	v_mov_b64_e32 v[74:75], s[8:9]
	v_mad_i64_i32 v[74:75], s[38:39], v76, s69, v[74:75]
	v_lshl_add_u64 v[74:75], v[122:123], 1, v[74:75]
	v_cvt_pk_bf16_f32 v76, v86, v87
	v_cvt_pk_bf16_f32 v77, v82, v83
	v_cvt_pk_bf16_f32 v78, v88, v89
	v_cvt_pk_bf16_f32 v79, v84, v85
	s_cmp_gt_i32 s29, 1
	s_mov_b64 s[38:39], -1
	global_store_dwordx4 v[74:75], v[76:79], off sc1
	s_cbranch_scc0 .LBB0_204
	s_nop 0
	v_mul_f32_e32 v76, 0xbfb8aa3b, v70
	v_exp_f32_e32 v76, v76
	v_mul_f32_e32 v77, 0xbfb8aa3b, v66
	v_mul_f32_e32 v78, 0xbfb8aa3b, v71
	v_exp_f32_e32 v77, v77
	v_exp_f32_e32 v79, v78
	v_add_f32_e32 v76, 1.0, v76
	v_rcp_f32_e32 v78, v76
	v_add_f32_e32 v76, 1.0, v77
	v_rcp_f32_e32 v82, v76
	v_add_f32_e32 v76, 1.0, v79
	v_rcp_f32_e32 v79, v76
	v_mul_f32_e32 v76, 0xbfb8aa3b, v67
	v_mul_f32_e32 v77, 0xbfb8aa3b, v72
	v_mul_f32_e32 v80, 0xbfb8aa3b, v68
	v_exp_f32_e32 v76, v76
	v_exp_f32_e32 v77, v77
	v_exp_f32_e32 v80, v80
	v_mul_f32_e32 v83, 0xbfb8aa3b, v69
	v_add_f32_e32 v81, 1.0, v76
	v_add_f32_e32 v76, 1.0, v77
	v_add_f32_e32 v77, 1.0, v80
	v_mul_f32_e32 v80, 0xbfb8aa3b, v73
	v_exp_f32_e32 v80, v80
	v_exp_f32_e32 v83, v83
	v_rcp_f32_e32 v84, v77
	v_rcp_f32_e32 v76, v76
	v_add_f32_e32 v77, 1.0, v80
	v_add_f32_e32 v80, 1.0, v83
	v_rcp_f32_e32 v77, v77
	v_rcp_f32_e32 v85, v80
	v_rcp_f32_e32 v83, v81
	v_pk_mul_f32 v[80:81], v[70:71], v[78:79]
	v_pk_mul_f32 v[76:77], v[72:73], v[76:77]
	v_pk_mul_f32 v[78:79], v[68:69], v[84:85]
	v_pk_mul_f32 v[82:83], v[66:67], v[82:83]
	s_mov_b64 s[38:39], 0

.LBB0_208:
	v_cvt_pk_bf16_f32 v66, v80, v81
	v_cvt_pk_bf16_f32 v67, v76, v77
	v_cvt_pk_bf16_f32 v68, v82, v83
	v_cvt_pk_bf16_f32 v69, v78, v79
	s_cmp_gt_i32 s29, 1
	s_mov_b64 s[38:39], -1
	global_store_dwordx4 v[74:75], v[66:69], off offset:256 sc1
	s_cbranch_scc0 .LBB0_210
	s_nop 0
	v_mul_f32_e32 v66, 0xbfb8aa3b, v62
	v_exp_f32_e32 v66, v66
	v_mul_f32_e32 v67, 0xbfb8aa3b, v58
	v_mul_f32_e32 v68, 0xbfb8aa3b, v63
	v_exp_f32_e32 v67, v67
	v_exp_f32_e32 v69, v68
	v_add_f32_e32 v66, 1.0, v66
	v_rcp_f32_e32 v68, v66
	v_add_f32_e32 v66, 1.0, v67
	v_rcp_f32_e32 v72, v66
	v_add_f32_e32 v66, 1.0, v69
	v_rcp_f32_e32 v69, v66
	v_mul_f32_e32 v66, 0xbfb8aa3b, v59
	v_mul_f32_e32 v67, 0xbfb8aa3b, v64
	v_mul_f32_e32 v70, 0xbfb8aa3b, v60
	v_exp_f32_e32 v66, v66
	v_exp_f32_e32 v67, v67
	v_exp_f32_e32 v70, v70
	v_mul_f32_e32 v73, 0xbfb8aa3b, v61
	v_add_f32_e32 v71, 1.0, v66
	v_add_f32_e32 v66, 1.0, v67
	v_add_f32_e32 v67, 1.0, v70
	v_mul_f32_e32 v70, 0xbfb8aa3b, v65
	v_exp_f32_e32 v70, v70
	v_exp_f32_e32 v73, v73
	v_rcp_f32_e32 v74, v67
	v_rcp_f32_e32 v66, v66
	v_add_f32_e32 v67, 1.0, v70
	v_add_f32_e32 v70, 1.0, v73
	v_rcp_f32_e32 v67, v67
	v_rcp_f32_e32 v75, v70
	v_rcp_f32_e32 v73, v71
	v_pk_mul_f32 v[70:71], v[62:63], v[68:69]
	v_pk_mul_f32 v[66:67], v[64:65], v[66:67]
	v_pk_mul_f32 v[68:69], v[60:61], v[74:75]
	v_pk_mul_f32 v[72:73], v[58:59], v[72:73]
	s_mov_b64 s[38:39], 0

.LBB0_214:
	v_add_u32_e32 v60, 0x80, v177
	v_mov_b64_e32 v[58:59], s[8:9]
	v_mad_i64_i32 v[58:59], s[38:39], v60, s69, v[58:59]
	v_lshl_add_u64 v[58:59], v[122:123], 1, v[58:59]
	v_cvt_pk_bf16_f32 v60, v70, v71
	v_cvt_pk_bf16_f32 v61, v66, v67
	v_cvt_pk_bf16_f32 v62, v72, v73
	v_cvt_pk_bf16_f32 v63, v68, v69
	s_cmp_gt_i32 s29, 1
	s_mov_b64 s[38:39], -1
	global_store_dwordx4 v[58:59], v[60:63], off sc1
	s_cbranch_scc0 .LBB0_216
	s_nop 0
	v_mul_f32_e32 v60, 0xbfb8aa3b, v54
	v_exp_f32_e32 v60, v60
	v_mul_f32_e32 v61, 0xbfb8aa3b, v50
	v_mul_f32_e32 v62, 0xbfb8aa3b, v55
	v_exp_f32_e32 v61, v61
	v_exp_f32_e32 v63, v62
	v_add_f32_e32 v60, 1.0, v60
	v_rcp_f32_e32 v62, v60
	v_add_f32_e32 v60, 1.0, v61
	v_rcp_f32_e32 v66, v60
	v_add_f32_e32 v60, 1.0, v63
	v_rcp_f32_e32 v63, v60
	v_mul_f32_e32 v60, 0xbfb8aa3b, v51
	v_mul_f32_e32 v61, 0xbfb8aa3b, v56
	v_mul_f32_e32 v64, 0xbfb8aa3b, v52
	v_exp_f32_e32 v60, v60
	v_exp_f32_e32 v61, v61
	v_exp_f32_e32 v64, v64
	v_mul_f32_e32 v67, 0xbfb8aa3b, v53
	v_add_f32_e32 v65, 1.0, v60
	v_add_f32_e32 v60, 1.0, v61
	v_add_f32_e32 v61, 1.0, v64
	v_mul_f32_e32 v64, 0xbfb8aa3b, v57
	v_exp_f32_e32 v64, v64
	v_exp_f32_e32 v67, v67
	v_rcp_f32_e32 v68, v61
	v_rcp_f32_e32 v60, v60
	v_add_f32_e32 v61, 1.0, v64
	v_add_f32_e32 v64, 1.0, v67
	v_rcp_f32_e32 v61, v61
	v_rcp_f32_e32 v69, v64
	v_rcp_f32_e32 v67, v65
	v_pk_mul_f32 v[64:65], v[54:55], v[62:63]
	v_pk_mul_f32 v[60:61], v[56:57], v[60:61]
	v_pk_mul_f32 v[62:63], v[52:53], v[68:69]
	v_pk_mul_f32 v[66:67], v[50:51], v[66:67]
	s_mov_b64 s[38:39], 0

.LBB0_220:
	v_cvt_pk_bf16_f32 v50, v64, v65
	v_cvt_pk_bf16_f32 v51, v60, v61
	v_cvt_pk_bf16_f32 v52, v66, v67
	v_cvt_pk_bf16_f32 v53, v62, v63
	s_cmp_gt_i32 s29, 1
	s_mov_b64 s[38:39], -1
	global_store_dwordx4 v[58:59], v[50:53], off offset:256 sc1
	s_cbranch_scc0 .LBB0_222
	s_nop 0
	v_mul_f32_e32 v50, 0xbfb8aa3b, v46
	v_exp_f32_e32 v50, v50
	v_mul_f32_e32 v51, 0xbfb8aa3b, v42
	v_mul_f32_e32 v52, 0xbfb8aa3b, v47
	v_exp_f32_e32 v51, v51
	v_exp_f32_e32 v53, v52
	v_add_f32_e32 v50, 1.0, v50
	v_rcp_f32_e32 v52, v50
	v_add_f32_e32 v50, 1.0, v51
	v_rcp_f32_e32 v56, v50
	v_add_f32_e32 v50, 1.0, v53
	v_rcp_f32_e32 v53, v50
	v_mul_f32_e32 v50, 0xbfb8aa3b, v43
	v_mul_f32_e32 v51, 0xbfb8aa3b, v48
	v_mul_f32_e32 v54, 0xbfb8aa3b, v44
	v_exp_f32_e32 v50, v50
	v_exp_f32_e32 v51, v51
	v_exp_f32_e32 v54, v54
	v_mul_f32_e32 v57, 0xbfb8aa3b, v45
	v_add_f32_e32 v55, 1.0, v50
	v_add_f32_e32 v50, 1.0, v51
	v_add_f32_e32 v51, 1.0, v54
	v_mul_f32_e32 v54, 0xbfb8aa3b, v49
	v_exp_f32_e32 v54, v54
	v_exp_f32_e32 v57, v57
	v_rcp_f32_e32 v58, v51
	v_rcp_f32_e32 v50, v50
	v_add_f32_e32 v51, 1.0, v54
	v_add_f32_e32 v54, 1.0, v57
	v_rcp_f32_e32 v51, v51
	v_rcp_f32_e32 v59, v54
	v_rcp_f32_e32 v57, v55
	v_pk_mul_f32 v[54:55], v[46:47], v[52:53]
	v_pk_mul_f32 v[50:51], v[48:49], v[50:51]
	v_pk_mul_f32 v[52:53], v[44:45], v[58:59]
	v_pk_mul_f32 v[56:57], v[42:43], v[56:57]
	s_mov_b64 s[38:39], 0

.LBB0_226:
	v_add_u32_e32 v44, 0x90, v177
	v_mov_b64_e32 v[42:43], s[8:9]
	v_mad_i64_i32 v[42:43], s[38:39], v44, s69, v[42:43]
	v_lshl_add_u64 v[42:43], v[122:123], 1, v[42:43]
	v_cvt_pk_bf16_f32 v44, v54, v55
	v_cvt_pk_bf16_f32 v45, v50, v51
	v_cvt_pk_bf16_f32 v46, v56, v57
	v_cvt_pk_bf16_f32 v47, v52, v53
	s_cmp_gt_i32 s29, 1
	s_mov_b64 s[38:39], -1
	global_store_dwordx4 v[42:43], v[44:47], off sc1
	s_cbranch_scc0 .LBB0_228
	s_nop 0
	v_mul_f32_e32 v44, 0xbfb8aa3b, v38
	v_exp_f32_e32 v44, v44
	v_mul_f32_e32 v45, 0xbfb8aa3b, v34
	v_mul_f32_e32 v46, 0xbfb8aa3b, v39
	v_exp_f32_e32 v45, v45
	v_exp_f32_e32 v47, v46
	v_add_f32_e32 v44, 1.0, v44
	v_rcp_f32_e32 v46, v44
	v_add_f32_e32 v44, 1.0, v45
	v_rcp_f32_e32 v50, v44
	v_add_f32_e32 v44, 1.0, v47
	v_rcp_f32_e32 v47, v44
	v_mul_f32_e32 v44, 0xbfb8aa3b, v35
	v_mul_f32_e32 v45, 0xbfb8aa3b, v40
	v_mul_f32_e32 v48, 0xbfb8aa3b, v36
	v_exp_f32_e32 v44, v44
	v_exp_f32_e32 v45, v45
	v_exp_f32_e32 v48, v48
	v_mul_f32_e32 v51, 0xbfb8aa3b, v37
	v_add_f32_e32 v49, 1.0, v44
	v_add_f32_e32 v44, 1.0, v45
	v_add_f32_e32 v45, 1.0, v48
	v_mul_f32_e32 v48, 0xbfb8aa3b, v41
	v_exp_f32_e32 v48, v48
	v_exp_f32_e32 v51, v51
	v_rcp_f32_e32 v52, v45
	v_rcp_f32_e32 v44, v44
	v_add_f32_e32 v45, 1.0, v48
	v_add_f32_e32 v48, 1.0, v51
	v_rcp_f32_e32 v45, v45
	v_rcp_f32_e32 v53, v48
	v_rcp_f32_e32 v51, v49
	v_pk_mul_f32 v[48:49], v[38:39], v[46:47]
	v_pk_mul_f32 v[44:45], v[40:41], v[44:45]
	v_pk_mul_f32 v[46:47], v[36:37], v[52:53]
	v_pk_mul_f32 v[50:51], v[34:35], v[50:51]
	s_mov_b64 s[38:39], 0

.LBB0_232:
	v_cvt_pk_bf16_f32 v34, v48, v49
	v_cvt_pk_bf16_f32 v35, v44, v45
	v_cvt_pk_bf16_f32 v36, v50, v51
	v_cvt_pk_bf16_f32 v37, v46, v47
	s_cmp_gt_i32 s29, 1
	s_mov_b64 s[38:39], -1
	global_store_dwordx4 v[42:43], v[34:37], off offset:256 sc1
	s_cbranch_scc0 .LBB0_234
	s_nop 0
	v_mul_f32_e32 v34, 0xbfb8aa3b, v30
	v_exp_f32_e32 v34, v34
	v_mul_f32_e32 v35, 0xbfb8aa3b, v26
	v_mul_f32_e32 v36, 0xbfb8aa3b, v31
	v_exp_f32_e32 v35, v35
	v_exp_f32_e32 v37, v36
	v_add_f32_e32 v34, 1.0, v34
	v_rcp_f32_e32 v36, v34
	v_add_f32_e32 v34, 1.0, v35
	v_rcp_f32_e32 v40, v34
	v_add_f32_e32 v34, 1.0, v37
	v_rcp_f32_e32 v37, v34
	v_mul_f32_e32 v34, 0xbfb8aa3b, v27
	v_mul_f32_e32 v35, 0xbfb8aa3b, v32
	v_mul_f32_e32 v38, 0xbfb8aa3b, v28
	v_exp_f32_e32 v34, v34
	v_exp_f32_e32 v35, v35
	v_exp_f32_e32 v38, v38
	v_mul_f32_e32 v41, 0xbfb8aa3b, v29
	v_add_f32_e32 v39, 1.0, v34
	v_add_f32_e32 v34, 1.0, v35
	v_add_f32_e32 v35, 1.0, v38
	v_mul_f32_e32 v38, 0xbfb8aa3b, v33
	v_exp_f32_e32 v38, v38
	v_exp_f32_e32 v41, v41
	v_rcp_f32_e32 v42, v35
	v_rcp_f32_e32 v34, v34
	v_add_f32_e32 v35, 1.0, v38
	v_add_f32_e32 v38, 1.0, v41
	v_rcp_f32_e32 v35, v35
	v_rcp_f32_e32 v43, v38
	v_rcp_f32_e32 v41, v39
	v_pk_mul_f32 v[38:39], v[30:31], v[36:37]
	v_pk_mul_f32 v[34:35], v[32:33], v[34:35]
	v_pk_mul_f32 v[36:37], v[28:29], v[42:43]
	v_pk_mul_f32 v[40:41], v[26:27], v[40:41]
	s_mov_b64 s[38:39], 0

.LBB0_238:
	v_add_u32_e32 v28, 0xa0, v177
	v_mov_b64_e32 v[26:27], s[8:9]
	v_mad_i64_i32 v[26:27], s[38:39], v28, s69, v[26:27]
	v_lshl_add_u64 v[26:27], v[122:123], 1, v[26:27]
	v_cvt_pk_bf16_f32 v28, v38, v39
	v_cvt_pk_bf16_f32 v29, v34, v35
	v_cvt_pk_bf16_f32 v30, v40, v41
	v_cvt_pk_bf16_f32 v31, v36, v37
	s_cmp_gt_i32 s29, 1
	s_mov_b64 s[38:39], -1
	global_store_dwordx4 v[26:27], v[28:31], off sc1
	s_cbranch_scc0 .LBB0_240
	s_nop 0
	v_mul_f32_e32 v28, 0xbfb8aa3b, v18
	v_exp_f32_e32 v28, v28
	v_mul_f32_e32 v29, 0xbfb8aa3b, v22
	v_mul_f32_e32 v30, 0xbfb8aa3b, v19
	v_exp_f32_e32 v29, v29
	v_exp_f32_e32 v31, v30
	v_add_f32_e32 v28, 1.0, v28
	v_rcp_f32_e32 v30, v28
	v_add_f32_e32 v28, 1.0, v29
	v_rcp_f32_e32 v34, v28
	v_add_f32_e32 v28, 1.0, v31
	v_rcp_f32_e32 v31, v28
	v_mul_f32_e32 v28, 0xbfb8aa3b, v23
	v_mul_f32_e32 v29, 0xbfb8aa3b, v20
	v_mul_f32_e32 v32, 0xbfb8aa3b, v24
	v_exp_f32_e32 v28, v28
	v_exp_f32_e32 v29, v29
	v_exp_f32_e32 v32, v32
	v_mul_f32_e32 v35, 0xbfb8aa3b, v25
	v_add_f32_e32 v33, 1.0, v28
	v_add_f32_e32 v28, 1.0, v29
	v_add_f32_e32 v29, 1.0, v32
	v_mul_f32_e32 v32, 0xbfb8aa3b, v21
	v_exp_f32_e32 v32, v32
	v_exp_f32_e32 v35, v35
	v_rcp_f32_e32 v36, v29
	v_rcp_f32_e32 v28, v28
	v_add_f32_e32 v29, 1.0, v32
	v_add_f32_e32 v32, 1.0, v35
	v_rcp_f32_e32 v29, v29
	v_rcp_f32_e32 v37, v32
	v_rcp_f32_e32 v35, v33
	v_pk_mul_f32 v[32:33], v[18:19], v[30:31]
	v_pk_mul_f32 v[28:29], v[20:21], v[28:29]
	v_pk_mul_f32 v[30:31], v[24:25], v[36:37]
	v_pk_mul_f32 v[34:35], v[22:23], v[34:35]
	s_mov_b64 s[38:39], 0

.LBB0_244:
	v_cvt_pk_bf16_f32 v18, v32, v33
	v_cvt_pk_bf16_f32 v19, v28, v29
	v_cvt_pk_bf16_f32 v20, v34, v35
	v_cvt_pk_bf16_f32 v21, v30, v31
	s_cmp_gt_i32 s29, 1
	s_mov_b64 s[38:39], -1
	global_store_dwordx4 v[26:27], v[18:21], off offset:256 sc1
	s_cbranch_scc0 .LBB0_246
	s_nop 0
	v_mul_f32_e32 v18, 0xbfb8aa3b, v14
	v_exp_f32_e32 v18, v18
	v_mul_f32_e32 v19, 0xbfb8aa3b, v10
	v_mul_f32_e32 v20, 0xbfb8aa3b, v15
	v_exp_f32_e32 v19, v19
	v_exp_f32_e32 v21, v20
	v_add_f32_e32 v18, 1.0, v18
	v_rcp_f32_e32 v20, v18
	v_add_f32_e32 v18, 1.0, v19
	v_rcp_f32_e32 v24, v18
	v_add_f32_e32 v18, 1.0, v21
	v_rcp_f32_e32 v21, v18
	v_mul_f32_e32 v18, 0xbfb8aa3b, v11
	v_mul_f32_e32 v19, 0xbfb8aa3b, v16
	v_mul_f32_e32 v22, 0xbfb8aa3b, v12
	v_exp_f32_e32 v18, v18
	v_exp_f32_e32 v19, v19
	v_exp_f32_e32 v22, v22
	v_mul_f32_e32 v25, 0xbfb8aa3b, v13
	v_add_f32_e32 v23, 1.0, v18
	v_add_f32_e32 v18, 1.0, v19
	v_add_f32_e32 v19, 1.0, v22
	v_mul_f32_e32 v22, 0xbfb8aa3b, v17
	v_exp_f32_e32 v22, v22
	v_exp_f32_e32 v25, v25
	v_rcp_f32_e32 v26, v19
	v_rcp_f32_e32 v18, v18
	v_add_f32_e32 v19, 1.0, v22
	v_add_f32_e32 v22, 1.0, v25
	v_rcp_f32_e32 v19, v19
	v_rcp_f32_e32 v27, v22
	v_rcp_f32_e32 v25, v23
	v_pk_mul_f32 v[22:23], v[14:15], v[20:21]
	v_pk_mul_f32 v[18:19], v[16:17], v[18:19]
	v_pk_mul_f32 v[20:21], v[12:13], v[26:27]
	v_pk_mul_f32 v[24:25], v[10:11], v[24:25]
	s_mov_b64 s[38:39], 0

.LBB0_250:
	v_add_u32_e32 v12, 0xb0, v177
	v_mov_b64_e32 v[10:11], s[8:9]
	v_mad_i64_i32 v[10:11], s[38:39], v12, s69, v[10:11]
	v_lshl_add_u64 v[10:11], v[122:123], 1, v[10:11]
	v_cvt_pk_bf16_f32 v12, v22, v23
	v_cvt_pk_bf16_f32 v13, v18, v19
	v_cvt_pk_bf16_f32 v14, v24, v25
	v_cvt_pk_bf16_f32 v15, v20, v21
	s_cmp_gt_i32 s29, 1
	s_mov_b64 s[38:39], -1
	global_store_dwordx4 v[10:11], v[12:15], off sc1
	s_cbranch_scc0 .LBB0_252
	s_nop 0
	v_mul_f32_e32 v12, 0xbfb8aa3b, v2
	v_exp_f32_e32 v12, v12
	v_mul_f32_e32 v13, 0xbfb8aa3b, v6
	v_mul_f32_e32 v14, 0xbfb8aa3b, v3
	v_exp_f32_e32 v13, v13
	v_exp_f32_e32 v15, v14
	v_add_f32_e32 v12, 1.0, v12
	v_rcp_f32_e32 v14, v12
	v_add_f32_e32 v12, 1.0, v13
	v_rcp_f32_e32 v18, v12
	v_add_f32_e32 v12, 1.0, v15
	v_rcp_f32_e32 v15, v12
	v_mul_f32_e32 v12, 0xbfb8aa3b, v7
	v_mul_f32_e32 v13, 0xbfb8aa3b, v4
	v_mul_f32_e32 v16, 0xbfb8aa3b, v8
	v_exp_f32_e32 v12, v12
	v_exp_f32_e32 v13, v13
	v_exp_f32_e32 v16, v16
	v_pk_mul_f32 v[14:15], v[2:3], v[14:15]
	v_add_f32_e32 v19, 1.0, v12
	v_add_f32_e32 v12, 1.0, v13
	v_add_f32_e32 v13, 1.0, v16
	v_mul_f32_e32 v16, 0xbfb8aa3b, v5
	v_exp_f32_e32 v17, v16
	v_mul_f32_e32 v16, 0xbfb8aa3b, v9
	v_exp_f32_e32 v20, v16
	v_rcp_f32_e32 v16, v13
	v_add_f32_e32 v13, 1.0, v17
	v_rcp_f32_e32 v12, v12
	v_add_f32_e32 v17, 1.0, v20
	v_rcp_f32_e32 v13, v13
	v_rcp_f32_e32 v17, v17
	v_rcp_f32_e32 v19, v19
	s_mov_b64 s[38:39], 0
	v_pk_mul_f32 v[12:13], v[4:5], v[12:13]
	v_pk_mul_f32 v[16:17], v[8:9], v[16:17]
	v_pk_mul_f32 v[18:19], v[6:7], v[18:19]

.LBB0_256:
	s_andn2_b64 vcc, exec, s[2:3]
	s_mov_b64 s[2:3], -1
	v_cvt_pk_bf16_f32 v2, v14, v15
	v_cvt_pk_bf16_f32 v3, v12, v13
	v_cvt_pk_bf16_f32 v4, v18, v19
	v_cvt_pk_bf16_f32 v5, v16, v17
	global_store_dwordx4 v[10:11], v[2:5], off offset:256 sc1
	s_cbranch_vccnz .LBB0_153
	s_andn2_b64 vcc, exec, s[4:5]
	s_cbranch_vccnz .LBB0_152
	s_barrier
	s_branch .LBB0_152

.LBB0_537:
	v_lshl_add_u32 v172, s30, 8, v1
	v_lshl_or_b32 v150, s69, 8, v169
	v_ashrrev_i32_e32 v173, 31, v172
	v_ashrrev_i32_e32 v151, 31, v150
	v_lshlrev_b64 v[174:175], 12, v[172:173]
	v_lshl_add_u64 v[174:175], s[10:11], 0, v[174:175]
	v_lshlrev_b64 v[176:177], 1, v[150:151]
	v_lshl_add_u64 v[150:151], v[174:175], 0, v[176:177]
	v_cvt_pk_bf16_f32 v126, v126, v127
	v_cvt_pk_bf16_f32 v127, v128, v129
	v_cvt_pk_bf16_f32 v128, v122, v123
	v_cvt_pk_bf16_f32 v129, v124, v125
	global_store_dwordx4 v[150:151], v[126:129], off sc1
	v_cvt_pk_bf16_f32 v114, v114, v115
	v_cvt_pk_bf16_f32 v115, v116, v117
	v_cvt_pk_bf16_f32 v116, v106, v107
	v_or_b32_e32 v106, 16, v172
	v_ashrrev_i32_e32 v107, 31, v106
	v_lshlrev_b64 v[106:107], 12, v[106:107]
	v_lshl_add_u64 v[106:107], s[10:11], 0, v[106:107]
	v_cvt_pk_bf16_f32 v117, v108, v109
	global_store_dwordx4 v[150:151], v[114:117], off offset:256 sc1
	s_nop 1
	v_lshl_add_u64 v[114:115], v[106:107], 0, v[176:177]
	v_cvt_pk_bf16_f32 v106, v118, v119
	v_cvt_pk_bf16_f32 v107, v120, v121
	v_cvt_pk_bf16_f32 v108, v110, v111
	v_cvt_pk_bf16_f32 v109, v112, v113
	global_store_dwordx4 v[114:115], v[106:109], off sc1
	v_cvt_pk_bf16_f32 v98, v98, v99
	v_cvt_pk_bf16_f32 v99, v100, v101
	v_cvt_pk_bf16_f32 v100, v90, v91
	v_or_b32_e32 v90, 32, v172
	v_ashrrev_i32_e32 v91, 31, v90
	v_lshlrev_b64 v[90:91], 12, v[90:91]
	v_lshl_add_u64 v[90:91], s[10:11], 0, v[90:91]
	v_cvt_pk_bf16_f32 v101, v92, v93
	global_store_dwordx4 v[114:115], v[98:101], off offset:256 sc1
	s_nop 1
	v_lshl_add_u64 v[98:99], v[90:91], 0, v[176:177]
	v_cvt_pk_bf16_f32 v90, v102, v103
	v_cvt_pk_bf16_f32 v91, v104, v105
	v_cvt_pk_bf16_f32 v92, v94, v95
	v_cvt_pk_bf16_f32 v93, v96, v97
	global_store_dwordx4 v[98:99], v[90:93], off sc1
	v_cvt_pk_bf16_f32 v82, v82, v83
	v_cvt_pk_bf16_f32 v83, v84, v85
	v_cvt_pk_bf16_f32 v84, v74, v75
	v_or_b32_e32 v74, 48, v172
	v_ashrrev_i32_e32 v75, 31, v74
	v_lshlrev_b64 v[74:75], 12, v[74:75]
	v_lshl_add_u64 v[74:75], s[10:11], 0, v[74:75]
	v_cvt_pk_bf16_f32 v85, v76, v77
	global_store_dwordx4 v[98:99], v[82:85], off offset:256 sc1
	s_nop 1
	v_lshl_add_u64 v[82:83], v[74:75], 0, v[176:177]
	v_cvt_pk_bf16_f32 v74, v86, v87
	v_cvt_pk_bf16_f32 v75, v88, v89
	v_cvt_pk_bf16_f32 v76, v78, v79
	v_cvt_pk_bf16_f32 v77, v80, v81
	global_store_dwordx4 v[82:83], v[74:77], off sc1
	v_cvt_pk_bf16_f32 v70, v70, v71
	v_cvt_pk_bf16_f32 v71, v72, v73
	v_cvt_pk_bf16_f32 v72, v66, v67
	v_cvt_pk_bf16_f32 v73, v68, v69
	global_store_dwordx4 v[82:83], v[70:73], off offset:256 sc1
	v_cvt_pk_bf16_f32 v62, v62, v63
	v_cvt_pk_bf16_f32 v63, v64, v65
	v_cvt_pk_bf16_f32 v64, v58, v59
	v_add_co_u32_e32 v58, vcc, s55, v150
	v_lshl_add_u64 v[66:67], v[150:151], 0, s[6:7]
	s_nop 0
	v_addc_co_u32_e32 v59, vcc, 0, v151, vcc
	v_cvt_pk_bf16_f32 v65, v60, v61
	global_store_dwordx4 v[58:59], v[62:65], off sc1
	v_cvt_pk_bf16_f32 v42, v42, v43
	v_cvt_pk_bf16_f32 v43, v44, v45
	v_cvt_pk_bf16_f32 v44, v30, v31
	v_cvt_pk_bf16_f32 v45, v32, v33
	global_store_dwordx4 v[66:67], v[42:45], off offset:256 sc1
	v_cvt_pk_bf16_f32 v30, v46, v47
	v_cvt_pk_bf16_f32 v31, v48, v49
	v_cvt_pk_bf16_f32 v32, v38, v39
	v_add_co_u32_e32 v38, vcc, s66, v150
	s_nop 0
	v_lshl_add_u64 v[42:43], v[150:151], 0, s[16:17]
	v_addc_co_u32_e32 v39, vcc, 0, v151, vcc
	v_cvt_pk_bf16_f32 v33, v40, v41
	global_store_dwordx4 v[38:39], v[30:33], off sc1
	v_cvt_pk_bf16_f32 v18, v18, v19
	v_cvt_pk_bf16_f32 v19, v20, v21
	v_cvt_pk_bf16_f32 v20, v10, v11
	v_cvt_pk_bf16_f32 v21, v12, v13
	global_store_dwordx4 v[42:43], v[18:21], off offset:256 sc1
	v_cvt_pk_bf16_f32 v10, v22, v23
	v_cvt_pk_bf16_f32 v11, v24, v25
	v_cvt_pk_bf16_f32 v12, v14, v15
	v_add_co_u32_e32 v14, vcc, s67, v150
	s_nop 0
	v_lshl_add_u64 v[18:19], v[150:151], 0, s[18:19]
	v_cvt_pk_bf16_f32 v13, v16, v17
	v_addc_co_u32_e32 v15, vcc, 0, v151, vcc
	global_store_dwordx4 v[14:15], v[10:13], off sc1
	s_nop 1
	v_cvt_pk_bf16_f32 v10, v54, v55
	v_cvt_pk_bf16_f32 v11, v56, v57
	v_cvt_pk_bf16_f32 v12, v50, v51
	v_cvt_pk_bf16_f32 v13, v52, v53
	global_store_dwordx4 v[18:19], v[10:13], off offset:256 sc1
	v_cvt_pk_bf16_f32 v6, v6, v7
	v_cvt_pk_bf16_f32 v7, v8, v9
	v_cvt_pk_bf16_f32 v8, v2, v3
	v_add_co_u32_e32 v2, vcc, s68, v150
	s_nop 0
	v_lshl_add_u64 v[10:11], v[150:151], 0, s[20:21]
	v_addc_co_u32_e32 v3, vcc, 0, v151, vcc
	s_andn2_b64 vcc, exec, s[2:3]
	s_mov_b64 s[2:3], -1
	v_cvt_pk_bf16_f32 v9, v4, v5
	global_store_dwordx4 v[2:3], v[6:9], off sc1
	v_cvt_pk_bf16_f32 v2, v34, v35
	v_cvt_pk_bf16_f32 v3, v36, v37
	v_cvt_pk_bf16_f32 v4, v26, v27
	v_cvt_pk_bf16_f32 v5, v28, v29
	global_store_dwordx4 v[10:11], v[2:5], off offset:256 sc1
	s_cbranch_vccnz .LBB0_526
	s_andn2_b64 vcc, exec, s[8:9]
	s_cbranch_vccnz .LBB0_525
	s_barrier
	s_branch .LBB0_525
